# baseline (speedup 1.0000x reference)
.Lu0_1:
	ds_read_b64_tr_b16 v[178:179], v206 offset:24576
	ds_read_b64_tr_b16 v[180:181], v206 offset:25600
	s_waitcnt lgkmcnt(9)
	v_mfma_f32_32x32x16_f16 v[98:113], v[82:85], v[154:157], v[34:49]
	v_add_f32_e32 v224, v66, v74
	v_add_f32_e32 v225, v67, v75
	v_add_f32_e32 v226, v68, v76
	v_add_f32_e32 v227, v69, v77
	v_cvt_pk_f16_f32 v158, v66, v67
	v_cvt_pk_f16_f32 v159, v68, v69
	ds_read_b64_tr_b16 v[174:175], v207 offset:24576
	ds_read_b64_tr_b16 v[176:177], v207 offset:25600
	s_waitcnt lgkmcnt(10)
	v_mfma_f32_32x32x16_f16 v[82:97], v[170:173], v[154:157], v[34:49]
	v_add_f32_e32 v228, v70, v78
	v_add_f32_e32 v229, v71, v79
	v_add_f32_e32 v230, v72, v80
	v_add_f32_e32 v231, v73, v81
	v_cvt_pk_f16_f32 v160, v70, v71
	v_cvt_pk_f16_f32 v161, v72, v73
	ds_read_b64_tr_b16 v[170:171], v206 offset:26624
	ds_read_b64_tr_b16 v[172:173], v206 offset:27648
	s_waitcnt lgkmcnt(11)
	v_mfma_f32_32x32x16_f16 v[98:113], v[166:169], v[146:149], v[98:113]
	v_add_f32_e32 v224, v50, v224
	v_add_f32_e32 v225, v51, v225
	v_add_f32_e32 v226, v52, v226
	v_add_f32_e32 v227, v53, v227
	v_cvt_pk_f16_f32 v150, v74, v75
	v_cvt_pk_f16_f32 v151, v76, v77
	ds_read_b64_tr_b16 v[74:75], v207 offset:26624
	ds_read_b64_tr_b16 v[76:77], v207 offset:27648
	s_waitcnt lgkmcnt(12)
	v_mfma_f32_32x32x16_f16 v[82:97], v[162:165], v[146:149], v[82:97]
	v_add_f32_e32 v228, v54, v228
	v_add_f32_e32 v229, v55, v229
	v_add_f32_e32 v230, v56, v230
	v_add_f32_e32 v231, v57, v231
	v_cvt_pk_f16_f32 v152, v78, v79
	v_cvt_pk_f16_f32 v153, v80, v81
	ds_read_b64_tr_b16 v[70:71], v206 offset:28672
	ds_read_b64_tr_b16 v[72:73], v206 offset:29696
	s_waitcnt lgkmcnt(13)
	v_mfma_f32_32x32x16_f16 v[98:113], v[126:129], v[138:141], v[98:113]
	v_add_f32_e32 v224, v58, v224
	v_add_f32_e32 v225, v59, v225
	v_add_f32_e32 v226, v60, v226
	v_add_f32_e32 v227, v61, v227
	v_cvt_pk_f16_f32 v142, v50, v51
	v_cvt_pk_f16_f32 v143, v52, v53
	ds_read_b64_tr_b16 v[66:67], v207 offset:28672
	ds_read_b64_tr_b16 v[68:69], v207 offset:29696
	s_waitcnt lgkmcnt(14)
	v_mfma_f32_32x32x16_f16 v[82:97], v[122:125], v[138:141], v[82:97]
	v_add_f32_e32 v228, v62, v228
	v_add_f32_e32 v229, v63, v229
	v_add_f32_e32 v230, v64, v230
	v_add_f32_e32 v231, v65, v231
	v_cvt_pk_f16_f32 v144, v54, v55
	v_cvt_pk_f16_f32 v145, v56, v57
	ds_read_b64_tr_b16 v[54:55], v206 offset:30720
	ds_read_b64_tr_b16 v[56:57], v206 offset:31744
	s_waitcnt lgkmcnt(14)
	v_mfma_f32_32x32x16_f16 v[98:113], v[118:121], v[134:137], v[98:113]
	v_add_f32_e32 v224, v224, v228
	v_add_f32_e32 v225, v225, v229
	v_add_f32_e32 v226, v226, v230
	v_add_f32_e32 v227, v227, v231
	v_cvt_pk_f16_f32 v130, v58, v59
	v_cvt_pk_f16_f32 v131, v60, v61
	ds_read_b64_tr_b16 v[50:51], v207 offset:30720
	ds_read_b64_tr_b16 v[52:53], v207 offset:31744
	v_mfma_f32_32x32x16_f16 v[82:97], v[114:117], v[134:137], v[82:97]
	v_add_f32_e32 v224, v224, v225
	v_add_f32_e32 v226, v226, v227
	v_add_f32_e32 v60, v224, v226
	v_cvt_pk_f16_f32 v132, v62, v63
	v_cvt_pk_f16_f32 v133, v64, v65
	s_add_i32 s26, s42, s36
	s_mov_b32 m0, s26
	s_nop 0
	global_load_lds_dwordx4 v221, s[50:51]
	s_add_i32 s26, s39, s35
	s_mov_b32 m0, s26
	s_nop 0
	global_load_lds_dwordx4 v222, s[52:53]
	v_max_f32_e32 v58, v98, v99
	v_max3_f32 v59, v100, v101, v83
	v_max3_f32 v58, v58, v82, v84
	v_max3_f32 v58, v58, v85, v102
	v_max3_f32 v59, v59, v104, v105
	v_max3_f32 v58, v58, v103, v86
	v_max3_f32 v59, v59, v88, v89
	v_max3_f32 v58, v58, v87, v106
	v_max3_f32 v59, v59, v108, v109
	v_max3_f32 v58, v58, v107, v90
	v_max3_f32 v59, v59, v92, v93
	v_max3_f32 v58, v58, v91, v110
	v_max3_f32 v59, v59, v112, v113
	v_max3_f32 v58, v58, v111, v94
	v_max3_f32 v59, v59, v96, v97
	v_max3_f32 v58, v58, v95, v59
	v_add_f32_e32 v198, v183, v60
	v_cmp_lt_f32_e32 vcc, s41, v58
	s_cmp_lg_u64 vcc, 0
	s_cselect_b64 s[26:27], -1, 0
	s_cbranch_vccnz .Lu0_9

.Lu0_4:
	s_add_i32 s26, s39, 0x2000
	s_cmpk_lg_i32 s39, 0x4000
	s_cselect_b32 s43, s26, 0
	ds_read_b64_tr_b16 v[126:127], v206 offset:32768
	ds_read_b64_tr_b16 v[128:129], v206 offset:33792
	s_waitcnt lgkmcnt(9)
	v_mfma_f32_32x32x16_f16 v[66:81], v[58:61], v[154:157], v[34:49]
	v_add_f32_e32 v224, v98, v106
	v_add_f32_e32 v225, v99, v107
	v_add_f32_e32 v226, v100, v108
	v_add_f32_e32 v227, v101, v109
	v_cvt_pk_f16_f32 v158, v98, v99
	v_cvt_pk_f16_f32 v159, v100, v101
	ds_read_b64_tr_b16 v[122:123], v207 offset:32768
	ds_read_b64_tr_b16 v[124:125], v207 offset:33792
	s_waitcnt lgkmcnt(10)
	v_mfma_f32_32x32x16_f16 v[50:65], v[114:117], v[154:157], v[34:49]
	v_add_f32_e32 v228, v102, v110
	v_add_f32_e32 v229, v103, v111
	v_add_f32_e32 v230, v104, v112
	v_add_f32_e32 v231, v105, v113
	v_cvt_pk_f16_f32 v160, v102, v103
	v_cvt_pk_f16_f32 v161, v104, v105
	ds_read_b64_tr_b16 v[118:119], v206 offset:34816
	ds_read_b64_tr_b16 v[120:121], v206 offset:35840
	s_waitcnt lgkmcnt(11)
	v_mfma_f32_32x32x16_f16 v[66:81], v[182:185], v[146:149], v[66:81]
	v_add_f32_e32 v224, v82, v224
	v_add_f32_e32 v225, v83, v225
	v_add_f32_e32 v226, v84, v226
	v_add_f32_e32 v227, v85, v227
	v_cvt_pk_f16_f32 v150, v106, v107
	v_cvt_pk_f16_f32 v151, v108, v109
	ds_read_b64_tr_b16 v[114:115], v207 offset:34816
	ds_read_b64_tr_b16 v[116:117], v207 offset:35840
	s_waitcnt lgkmcnt(12)
	v_mfma_f32_32x32x16_f16 v[50:65], v[174:177], v[146:149], v[50:65]
	v_add_f32_e32 v228, v86, v228
	v_add_f32_e32 v229, v87, v229
	v_add_f32_e32 v230, v88, v230
	v_add_f32_e32 v231, v89, v231
	v_cvt_pk_f16_f32 v152, v110, v111
	v_cvt_pk_f16_f32 v153, v112, v113
	ds_read_b64_tr_b16 v[106:107], v206 offset:36864
	ds_read_b64_tr_b16 v[108:109], v206 offset:37888
	s_waitcnt lgkmcnt(13)
	v_mfma_f32_32x32x16_f16 v[66:81], v[178:181], v[138:141], v[66:81]
	v_add_f32_e32 v224, v90, v224
	v_add_f32_e32 v225, v91, v225
	v_add_f32_e32 v226, v92, v226
	v_add_f32_e32 v227, v93, v227
	v_cvt_pk_f16_f32 v142, v82, v83
	v_cvt_pk_f16_f32 v143, v84, v85
	ds_read_b64_tr_b16 v[102:103], v207 offset:36864
	ds_read_b64_tr_b16 v[104:105], v207 offset:37888
	s_waitcnt lgkmcnt(14)
	v_mfma_f32_32x32x16_f16 v[50:65], v[166:169], v[138:141], v[50:65]
	v_add_f32_e32 v228, v94, v228
	v_add_f32_e32 v229, v95, v229
	v_add_f32_e32 v230, v96, v230
	v_add_f32_e32 v231, v97, v231
	v_cvt_pk_f16_f32 v144, v86, v87
	v_cvt_pk_f16_f32 v145, v88, v89
	ds_read_b64_tr_b16 v[98:99], v206 offset:38912
	ds_read_b64_tr_b16 v[100:101], v206 offset:39936
	s_waitcnt lgkmcnt(14)
	v_mfma_f32_32x32x16_f16 v[66:81], v[170:173], v[134:137], v[66:81]
	v_add_f32_e32 v224, v224, v228
	v_add_f32_e32 v225, v225, v229
	v_add_f32_e32 v226, v226, v230
	v_add_f32_e32 v227, v227, v231
	v_cvt_pk_f16_f32 v130, v90, v91
	v_cvt_pk_f16_f32 v131, v92, v93
	ds_read_b64_tr_b16 v[86:87], v207 offset:38912
	ds_read_b64_tr_b16 v[88:89], v207 offset:39936
	v_mfma_f32_32x32x16_f16 v[50:65], v[162:165], v[134:137], v[50:65]
	v_add_f32_e32 v224, v224, v225
	v_add_f32_e32 v226, v226, v227
	v_add_f32_e32 v84, v224, v226
	v_cvt_pk_f16_f32 v132, v94, v95
	v_cvt_pk_f16_f32 v133, v96, v97
	s_add_u32 s54, s50, 0x2000
	s_addc_u32 s55, s51, 0
	s_add_i32 s26, s39, s36
	s_mov_b32 m0, s26
	s_nop 0
	global_load_lds_dwordx4 v221, s[54:55]
	v_max_f32_e32 v82, v66, v67
	s_nop 1
	v_max3_f32 v83, v68, v69, v51
	v_max3_f32 v82, v82, v50, v52
	v_max3_f32 v82, v82, v53, v70
	v_max3_f32 v83, v83, v72, v73
	v_max3_f32 v82, v82, v71, v54
	v_max3_f32 v83, v83, v56, v57
	v_max3_f32 v82, v82, v55, v74
	v_max3_f32 v83, v83, v76, v77
	v_max3_f32 v82, v82, v75, v58
	v_max3_f32 v83, v83, v60, v61
	v_max3_f32 v82, v82, v59, v78
	v_max3_f32 v83, v83, v80, v81
	v_max3_f32 v82, v82, v79, v62
	v_max3_f32 v83, v83, v64, v65
	v_max3_f32 v82, v82, v63, v83
	v_add_f32_e32 v183, v198, v84
	s_add_u32 s54, s52, 0x2000
	s_addc_u32 s55, s53, 0
	s_add_i32 s26, s43, s35
	s_mov_b32 m0, s26
	s_nop 0
	global_load_lds_dwordx4 v222, s[54:55]
	v_cmp_lt_f32_e32 vcc, s41, v82
	s_cmp_lg_u64 vcc, 0
	s_cselect_b64 s[26:27], -1, 0
	s_cbranch_vccnz .Lu0_12

.Lu1_1:
	ds_read_b64_tr_b16 v[178:179], v206 offset:40960
	ds_read_b64_tr_b16 v[180:181], v206 offset:41984
	s_waitcnt lgkmcnt(9)
	v_mfma_f32_32x32x16_f16 v[98:113], v[82:85], v[154:157], v[34:49]
	v_add_f32_e32 v224, v66, v74
	v_add_f32_e32 v225, v67, v75
	v_add_f32_e32 v226, v68, v76
	v_add_f32_e32 v227, v69, v77
	v_cvt_pk_f16_f32 v158, v66, v67
	v_cvt_pk_f16_f32 v159, v68, v69
	ds_read_b64_tr_b16 v[174:175], v207 offset:40960
	ds_read_b64_tr_b16 v[176:177], v207 offset:41984
	s_waitcnt lgkmcnt(10)
	v_mfma_f32_32x32x16_f16 v[82:97], v[170:173], v[154:157], v[34:49]
	v_add_f32_e32 v228, v70, v78
	v_add_f32_e32 v229, v71, v79
	v_add_f32_e32 v230, v72, v80
	v_add_f32_e32 v231, v73, v81
	v_cvt_pk_f16_f32 v160, v70, v71
	v_cvt_pk_f16_f32 v161, v72, v73
	ds_read_b64_tr_b16 v[170:171], v206 offset:43008
	ds_read_b64_tr_b16 v[172:173], v206 offset:44032
	s_waitcnt lgkmcnt(11)
	v_mfma_f32_32x32x16_f16 v[98:113], v[166:169], v[146:149], v[98:113]
	v_add_f32_e32 v224, v50, v224
	v_add_f32_e32 v225, v51, v225
	v_add_f32_e32 v226, v52, v226
	v_add_f32_e32 v227, v53, v227
	v_cvt_pk_f16_f32 v150, v74, v75
	v_cvt_pk_f16_f32 v151, v76, v77
	ds_read_b64_tr_b16 v[74:75], v207 offset:43008
	ds_read_b64_tr_b16 v[76:77], v207 offset:44032
	s_waitcnt lgkmcnt(12)
	v_mfma_f32_32x32x16_f16 v[82:97], v[162:165], v[146:149], v[82:97]
	v_add_f32_e32 v228, v54, v228
	v_add_f32_e32 v229, v55, v229
	v_add_f32_e32 v230, v56, v230
	v_add_f32_e32 v231, v57, v231
	v_cvt_pk_f16_f32 v152, v78, v79
	v_cvt_pk_f16_f32 v153, v80, v81
	ds_read_b64_tr_b16 v[70:71], v206 offset:45056
	ds_read_b64_tr_b16 v[72:73], v206 offset:46080
	s_waitcnt lgkmcnt(13)
	v_mfma_f32_32x32x16_f16 v[98:113], v[126:129], v[138:141], v[98:113]
	v_add_f32_e32 v224, v58, v224
	v_add_f32_e32 v225, v59, v225
	v_add_f32_e32 v226, v60, v226
	v_add_f32_e32 v227, v61, v227
	v_cvt_pk_f16_f32 v142, v50, v51
	v_cvt_pk_f16_f32 v143, v52, v53
	ds_read_b64_tr_b16 v[66:67], v207 offset:45056
	ds_read_b64_tr_b16 v[68:69], v207 offset:46080
	s_waitcnt lgkmcnt(14)
	v_mfma_f32_32x32x16_f16 v[82:97], v[122:125], v[138:141], v[82:97]
	v_add_f32_e32 v228, v62, v228
	v_add_f32_e32 v229, v63, v229
	v_add_f32_e32 v230, v64, v230
	v_add_f32_e32 v231, v65, v231
	v_cvt_pk_f16_f32 v144, v54, v55
	v_cvt_pk_f16_f32 v145, v56, v57
	ds_read_b64_tr_b16 v[54:55], v206 offset:47104
	ds_read_b64_tr_b16 v[56:57], v206 offset:48128
	s_waitcnt lgkmcnt(14)
	v_mfma_f32_32x32x16_f16 v[98:113], v[118:121], v[134:137], v[98:113]
	v_add_f32_e32 v224, v224, v228
	v_add_f32_e32 v225, v225, v229
	v_add_f32_e32 v226, v226, v230
	v_add_f32_e32 v227, v227, v231
	v_cvt_pk_f16_f32 v130, v58, v59
	v_cvt_pk_f16_f32 v131, v60, v61
	ds_read_b64_tr_b16 v[50:51], v207 offset:47104
	ds_read_b64_tr_b16 v[52:53], v207 offset:48128
	v_mfma_f32_32x32x16_f16 v[82:97], v[114:117], v[134:137], v[82:97]
	v_add_f32_e32 v224, v224, v225
	v_add_f32_e32 v226, v226, v227
	v_add_f32_e32 v60, v224, v226
	v_cvt_pk_f16_f32 v132, v62, v63
	v_cvt_pk_f16_f32 v133, v64, v65
	s_add_i32 s26, s42, s36
	s_mov_b32 m0, s26
	s_nop 0
	global_load_lds_dwordx4 v221, s[50:51]
	s_add_i32 s26, s39, s35
	s_mov_b32 m0, s26
	s_nop 0
	global_load_lds_dwordx4 v222, s[52:53]
	v_max_f32_e32 v58, v98, v99
	v_max3_f32 v59, v100, v101, v83
	v_max3_f32 v58, v58, v82, v84
	v_max3_f32 v58, v58, v85, v102
	v_max3_f32 v59, v59, v104, v105
	v_max3_f32 v58, v58, v103, v86
	v_max3_f32 v59, v59, v88, v89
	v_max3_f32 v58, v58, v87, v106
	v_max3_f32 v59, v59, v108, v109
	v_max3_f32 v58, v58, v107, v90
	v_max3_f32 v59, v59, v92, v93
	v_max3_f32 v58, v58, v91, v110
	v_max3_f32 v59, v59, v112, v113
	v_max3_f32 v58, v58, v111, v94
	v_max3_f32 v59, v59, v96, v97
	v_max3_f32 v58, v58, v95, v59
	v_add_f32_e32 v198, v183, v60
	v_cmp_lt_f32_e32 vcc, s41, v58
	s_cmp_lg_u64 vcc, 0
	s_cselect_b64 s[26:27], -1, 0
	s_cbranch_vccnz .Lu1_9

.Lu1_4:
	s_add_i32 s26, s39, 0x2000
	s_cmpk_lg_i32 s39, 0x4000
	s_cselect_b32 s43, s26, 0
	ds_read_b64_tr_b16 v[126:127], v206 offset:24576
	ds_read_b64_tr_b16 v[128:129], v206 offset:25600
	s_waitcnt lgkmcnt(9)
	v_mfma_f32_32x32x16_f16 v[66:81], v[58:61], v[154:157], v[34:49]
	v_add_f32_e32 v224, v98, v106
	v_add_f32_e32 v225, v99, v107
	v_add_f32_e32 v226, v100, v108
	v_add_f32_e32 v227, v101, v109
	v_cvt_pk_f16_f32 v158, v98, v99
	v_cvt_pk_f16_f32 v159, v100, v101
	ds_read_b64_tr_b16 v[122:123], v207 offset:24576
	ds_read_b64_tr_b16 v[124:125], v207 offset:25600
	s_waitcnt lgkmcnt(10)
	v_mfma_f32_32x32x16_f16 v[50:65], v[114:117], v[154:157], v[34:49]
	v_add_f32_e32 v228, v102, v110
	v_add_f32_e32 v229, v103, v111
	v_add_f32_e32 v230, v104, v112
	v_add_f32_e32 v231, v105, v113
	v_cvt_pk_f16_f32 v160, v102, v103
	v_cvt_pk_f16_f32 v161, v104, v105
	ds_read_b64_tr_b16 v[118:119], v206 offset:26624
	ds_read_b64_tr_b16 v[120:121], v206 offset:27648
	s_waitcnt lgkmcnt(11)
	v_mfma_f32_32x32x16_f16 v[66:81], v[182:185], v[146:149], v[66:81]
	v_add_f32_e32 v224, v82, v224
	v_add_f32_e32 v225, v83, v225
	v_add_f32_e32 v226, v84, v226
	v_add_f32_e32 v227, v85, v227
	v_cvt_pk_f16_f32 v150, v106, v107
	v_cvt_pk_f16_f32 v151, v108, v109
	ds_read_b64_tr_b16 v[114:115], v207 offset:26624
	ds_read_b64_tr_b16 v[116:117], v207 offset:27648
	s_waitcnt lgkmcnt(12)
	v_mfma_f32_32x32x16_f16 v[50:65], v[174:177], v[146:149], v[50:65]
	v_add_f32_e32 v228, v86, v228
	v_add_f32_e32 v229, v87, v229
	v_add_f32_e32 v230, v88, v230
	v_add_f32_e32 v231, v89, v231
	v_cvt_pk_f16_f32 v152, v110, v111
	v_cvt_pk_f16_f32 v153, v112, v113
	ds_read_b64_tr_b16 v[106:107], v206 offset:28672
	ds_read_b64_tr_b16 v[108:109], v206 offset:29696
	s_waitcnt lgkmcnt(13)
	v_mfma_f32_32x32x16_f16 v[66:81], v[178:181], v[138:141], v[66:81]
	v_add_f32_e32 v224, v90, v224
	v_add_f32_e32 v225, v91, v225
	v_add_f32_e32 v226, v92, v226
	v_add_f32_e32 v227, v93, v227
	v_cvt_pk_f16_f32 v142, v82, v83
	v_cvt_pk_f16_f32 v143, v84, v85
	ds_read_b64_tr_b16 v[102:103], v207 offset:28672
	ds_read_b64_tr_b16 v[104:105], v207 offset:29696
	s_waitcnt lgkmcnt(14)
	v_mfma_f32_32x32x16_f16 v[50:65], v[166:169], v[138:141], v[50:65]
	v_add_f32_e32 v228, v94, v228
	v_add_f32_e32 v229, v95, v229
	v_add_f32_e32 v230, v96, v230
	v_add_f32_e32 v231, v97, v231
	v_cvt_pk_f16_f32 v144, v86, v87
	v_cvt_pk_f16_f32 v145, v88, v89
	ds_read_b64_tr_b16 v[98:99], v206 offset:30720
	ds_read_b64_tr_b16 v[100:101], v206 offset:31744
	s_waitcnt lgkmcnt(14)
	v_mfma_f32_32x32x16_f16 v[66:81], v[170:173], v[134:137], v[66:81]
	v_add_f32_e32 v224, v224, v228
	v_add_f32_e32 v225, v225, v229
	v_add_f32_e32 v226, v226, v230
	v_add_f32_e32 v227, v227, v231
	v_cvt_pk_f16_f32 v130, v90, v91
	v_cvt_pk_f16_f32 v131, v92, v93
	ds_read_b64_tr_b16 v[86:87], v207 offset:30720
	ds_read_b64_tr_b16 v[88:89], v207 offset:31744
	v_mfma_f32_32x32x16_f16 v[50:65], v[162:165], v[134:137], v[50:65]
	v_add_f32_e32 v224, v224, v225
	v_add_f32_e32 v226, v226, v227
	v_add_f32_e32 v84, v224, v226
	v_cvt_pk_f16_f32 v132, v94, v95
	v_cvt_pk_f16_f32 v133, v96, v97
	s_add_u32 s54, s50, 0x2000
	s_addc_u32 s55, s51, 0
	s_add_i32 s26, s39, s36
	s_mov_b32 m0, s26
	s_nop 0
	global_load_lds_dwordx4 v221, s[54:55]
	v_max_f32_e32 v82, v66, v67
	s_nop 1
	v_max3_f32 v83, v68, v69, v51
	v_max3_f32 v82, v82, v50, v52
	v_max3_f32 v82, v82, v53, v70
	v_max3_f32 v83, v83, v72, v73
	v_max3_f32 v82, v82, v71, v54
	v_max3_f32 v83, v83, v56, v57
	v_max3_f32 v82, v82, v55, v74
	v_max3_f32 v83, v83, v76, v77
	v_max3_f32 v82, v82, v75, v58
	v_max3_f32 v83, v83, v60, v61
	v_max3_f32 v82, v82, v59, v78
	v_max3_f32 v83, v83, v80, v81
	v_max3_f32 v82, v82, v79, v62
	v_max3_f32 v83, v83, v64, v65
	v_max3_f32 v82, v82, v63, v83
	v_add_f32_e32 v183, v198, v84
	s_add_u32 s54, s52, 0x2000
	s_addc_u32 s55, s53, 0
	s_add_i32 s26, s43, s35
	s_mov_b32 m0, s26
	s_nop 0
	global_load_lds_dwordx4 v222, s[54:55]
	v_cmp_lt_f32_e32 vcc, s41, v82
	s_cmp_lg_u64 vcc, 0
	s_cselect_b64 s[26:27], -1, 0
	s_cbranch_vccnz .Lu1_12

.Lu2_1:
	ds_read_b64_tr_b16 v[178:179], v206 offset:32768
	ds_read_b64_tr_b16 v[180:181], v206 offset:33792
	s_waitcnt lgkmcnt(9)
	v_mfma_f32_32x32x16_f16 v[98:113], v[82:85], v[154:157], v[34:49]
	v_add_f32_e32 v224, v66, v74
	v_add_f32_e32 v225, v67, v75
	v_add_f32_e32 v226, v68, v76
	v_add_f32_e32 v227, v69, v77
	v_cvt_pk_f16_f32 v158, v66, v67
	v_cvt_pk_f16_f32 v159, v68, v69
	ds_read_b64_tr_b16 v[174:175], v207 offset:32768
	ds_read_b64_tr_b16 v[176:177], v207 offset:33792
	s_waitcnt lgkmcnt(10)
	v_mfma_f32_32x32x16_f16 v[82:97], v[170:173], v[154:157], v[34:49]
	v_add_f32_e32 v228, v70, v78
	v_add_f32_e32 v229, v71, v79
	v_add_f32_e32 v230, v72, v80
	v_add_f32_e32 v231, v73, v81
	v_cvt_pk_f16_f32 v160, v70, v71
	v_cvt_pk_f16_f32 v161, v72, v73
	ds_read_b64_tr_b16 v[170:171], v206 offset:34816
	ds_read_b64_tr_b16 v[172:173], v206 offset:35840
	s_waitcnt lgkmcnt(11)
	v_mfma_f32_32x32x16_f16 v[98:113], v[166:169], v[146:149], v[98:113]
	v_add_f32_e32 v224, v50, v224
	v_add_f32_e32 v225, v51, v225
	v_add_f32_e32 v226, v52, v226
	v_add_f32_e32 v227, v53, v227
	v_cvt_pk_f16_f32 v150, v74, v75
	v_cvt_pk_f16_f32 v151, v76, v77
	ds_read_b64_tr_b16 v[74:75], v207 offset:34816
	ds_read_b64_tr_b16 v[76:77], v207 offset:35840
	s_waitcnt lgkmcnt(12)
	v_mfma_f32_32x32x16_f16 v[82:97], v[162:165], v[146:149], v[82:97]
	v_add_f32_e32 v228, v54, v228
	v_add_f32_e32 v229, v55, v229
	v_add_f32_e32 v230, v56, v230
	v_add_f32_e32 v231, v57, v231
	v_cvt_pk_f16_f32 v152, v78, v79
	v_cvt_pk_f16_f32 v153, v80, v81
	ds_read_b64_tr_b16 v[70:71], v206 offset:36864
	ds_read_b64_tr_b16 v[72:73], v206 offset:37888
	s_waitcnt lgkmcnt(13)
	v_mfma_f32_32x32x16_f16 v[98:113], v[126:129], v[138:141], v[98:113]
	v_add_f32_e32 v224, v58, v224
	v_add_f32_e32 v225, v59, v225
	v_add_f32_e32 v226, v60, v226
	v_add_f32_e32 v227, v61, v227
	v_cvt_pk_f16_f32 v142, v50, v51
	v_cvt_pk_f16_f32 v143, v52, v53
	ds_read_b64_tr_b16 v[66:67], v207 offset:36864
	ds_read_b64_tr_b16 v[68:69], v207 offset:37888
	s_waitcnt lgkmcnt(14)
	v_mfma_f32_32x32x16_f16 v[82:97], v[122:125], v[138:141], v[82:97]
	v_add_f32_e32 v228, v62, v228
	v_add_f32_e32 v229, v63, v229
	v_add_f32_e32 v230, v64, v230
	v_add_f32_e32 v231, v65, v231
	v_cvt_pk_f16_f32 v144, v54, v55
	v_cvt_pk_f16_f32 v145, v56, v57
	ds_read_b64_tr_b16 v[54:55], v206 offset:38912
	ds_read_b64_tr_b16 v[56:57], v206 offset:39936
	s_waitcnt lgkmcnt(14)
	v_mfma_f32_32x32x16_f16 v[98:113], v[118:121], v[134:137], v[98:113]
	v_add_f32_e32 v224, v224, v228
	v_add_f32_e32 v225, v225, v229
	v_add_f32_e32 v226, v226, v230
	v_add_f32_e32 v227, v227, v231
	v_cvt_pk_f16_f32 v130, v58, v59
	v_cvt_pk_f16_f32 v131, v60, v61
	ds_read_b64_tr_b16 v[50:51], v207 offset:38912
	ds_read_b64_tr_b16 v[52:53], v207 offset:39936
	v_mfma_f32_32x32x16_f16 v[82:97], v[114:117], v[134:137], v[82:97]
	v_add_f32_e32 v224, v224, v225
	v_add_f32_e32 v226, v226, v227
	v_add_f32_e32 v60, v224, v226
	v_cvt_pk_f16_f32 v132, v62, v63
	v_cvt_pk_f16_f32 v133, v64, v65
	s_add_i32 s26, s42, s36
	s_mov_b32 m0, s26
	s_nop 0
	global_load_lds_dwordx4 v221, s[50:51]
	s_add_i32 s26, s39, s35
	s_mov_b32 m0, s26
	s_nop 0
	global_load_lds_dwordx4 v222, s[52:53]
	v_max_f32_e32 v58, v98, v99
	v_max3_f32 v59, v100, v101, v83
	v_max3_f32 v58, v58, v82, v84
	v_max3_f32 v58, v58, v85, v102
	v_max3_f32 v59, v59, v104, v105
	v_max3_f32 v58, v58, v103, v86
	v_max3_f32 v59, v59, v88, v89
	v_max3_f32 v58, v58, v87, v106
	v_max3_f32 v59, v59, v108, v109
	v_max3_f32 v58, v58, v107, v90
	v_max3_f32 v59, v59, v92, v93
	v_max3_f32 v58, v58, v91, v110
	v_max3_f32 v59, v59, v112, v113
	v_max3_f32 v58, v58, v111, v94
	v_max3_f32 v59, v59, v96, v97
	v_max3_f32 v58, v58, v95, v59
	v_add_f32_e32 v198, v183, v60
	v_cmp_lt_f32_e32 vcc, s41, v58
	s_cmp_lg_u64 vcc, 0
	s_cselect_b64 s[26:27], -1, 0
	s_cbranch_vccnz .Lu2_9

.Lu2_4:
	s_add_i32 s26, s39, 0x2000
	s_cmpk_lg_i32 s39, 0x4000
	s_cselect_b32 s43, s26, 0
	ds_read_b64_tr_b16 v[126:127], v206 offset:40960
	ds_read_b64_tr_b16 v[128:129], v206 offset:41984
	s_waitcnt lgkmcnt(9)
	v_mfma_f32_32x32x16_f16 v[66:81], v[58:61], v[154:157], v[34:49]
	v_add_f32_e32 v224, v98, v106
	v_add_f32_e32 v225, v99, v107
	v_add_f32_e32 v226, v100, v108
	v_add_f32_e32 v227, v101, v109
	v_cvt_pk_f16_f32 v158, v98, v99
	v_cvt_pk_f16_f32 v159, v100, v101
	ds_read_b64_tr_b16 v[122:123], v207 offset:40960
	ds_read_b64_tr_b16 v[124:125], v207 offset:41984
	s_waitcnt lgkmcnt(10)
	v_mfma_f32_32x32x16_f16 v[50:65], v[114:117], v[154:157], v[34:49]
	v_add_f32_e32 v228, v102, v110
	v_add_f32_e32 v229, v103, v111
	v_add_f32_e32 v230, v104, v112
	v_add_f32_e32 v231, v105, v113
	v_cvt_pk_f16_f32 v160, v102, v103
	v_cvt_pk_f16_f32 v161, v104, v105
	ds_read_b64_tr_b16 v[118:119], v206 offset:43008
	ds_read_b64_tr_b16 v[120:121], v206 offset:44032
	s_waitcnt lgkmcnt(11)
	v_mfma_f32_32x32x16_f16 v[66:81], v[182:185], v[146:149], v[66:81]
	v_add_f32_e32 v224, v82, v224
	v_add_f32_e32 v225, v83, v225
	v_add_f32_e32 v226, v84, v226
	v_add_f32_e32 v227, v85, v227
	v_cvt_pk_f16_f32 v150, v106, v107
	v_cvt_pk_f16_f32 v151, v108, v109
	ds_read_b64_tr_b16 v[114:115], v207 offset:43008
	ds_read_b64_tr_b16 v[116:117], v207 offset:44032
	s_waitcnt lgkmcnt(12)
	v_mfma_f32_32x32x16_f16 v[50:65], v[174:177], v[146:149], v[50:65]
	v_add_f32_e32 v228, v86, v228
	v_add_f32_e32 v229, v87, v229
	v_add_f32_e32 v230, v88, v230
	v_add_f32_e32 v231, v89, v231
	v_cvt_pk_f16_f32 v152, v110, v111
	v_cvt_pk_f16_f32 v153, v112, v113
	ds_read_b64_tr_b16 v[106:107], v206 offset:45056
	ds_read_b64_tr_b16 v[108:109], v206 offset:46080
	s_waitcnt lgkmcnt(13)
	v_mfma_f32_32x32x16_f16 v[66:81], v[178:181], v[138:141], v[66:81]
	v_add_f32_e32 v224, v90, v224
	v_add_f32_e32 v225, v91, v225
	v_add_f32_e32 v226, v92, v226
	v_add_f32_e32 v227, v93, v227
	v_cvt_pk_f16_f32 v142, v82, v83
	v_cvt_pk_f16_f32 v143, v84, v85
	ds_read_b64_tr_b16 v[102:103], v207 offset:45056
	ds_read_b64_tr_b16 v[104:105], v207 offset:46080
	s_waitcnt lgkmcnt(14)
	v_mfma_f32_32x32x16_f16 v[50:65], v[166:169], v[138:141], v[50:65]
	v_add_f32_e32 v228, v94, v228
	v_add_f32_e32 v229, v95, v229
	v_add_f32_e32 v230, v96, v230
	v_add_f32_e32 v231, v97, v231
	v_cvt_pk_f16_f32 v144, v86, v87
	v_cvt_pk_f16_f32 v145, v88, v89
	ds_read_b64_tr_b16 v[98:99], v206 offset:47104
	ds_read_b64_tr_b16 v[100:101], v206 offset:48128
	s_waitcnt lgkmcnt(14)
	v_mfma_f32_32x32x16_f16 v[66:81], v[170:173], v[134:137], v[66:81]
	v_add_f32_e32 v224, v224, v228
	v_add_f32_e32 v225, v225, v229
	v_add_f32_e32 v226, v226, v230
	v_add_f32_e32 v227, v227, v231
	v_cvt_pk_f16_f32 v130, v90, v91
	v_cvt_pk_f16_f32 v131, v92, v93
	ds_read_b64_tr_b16 v[86:87], v207 offset:47104
	ds_read_b64_tr_b16 v[88:89], v207 offset:48128
	v_mfma_f32_32x32x16_f16 v[50:65], v[162:165], v[134:137], v[50:65]
	v_add_f32_e32 v224, v224, v225
	v_add_f32_e32 v226, v226, v227
	v_add_f32_e32 v84, v224, v226
	v_cvt_pk_f16_f32 v132, v94, v95
	v_cvt_pk_f16_f32 v133, v96, v97
	s_add_u32 s54, s50, 0x2000
	s_addc_u32 s55, s51, 0
	s_add_i32 s26, s39, s36
	s_mov_b32 m0, s26
	s_nop 0
	global_load_lds_dwordx4 v221, s[54:55]
	v_max_f32_e32 v82, v66, v67
	s_nop 1
	v_max3_f32 v83, v68, v69, v51
	v_max3_f32 v82, v82, v50, v52
	v_max3_f32 v82, v82, v53, v70
	v_max3_f32 v83, v83, v72, v73
	v_max3_f32 v82, v82, v71, v54
	v_max3_f32 v83, v83, v56, v57
	v_max3_f32 v82, v82, v55, v74
	v_max3_f32 v83, v83, v76, v77
	v_max3_f32 v82, v82, v75, v58
	v_max3_f32 v83, v83, v60, v61
	v_max3_f32 v82, v82, v59, v78
	v_max3_f32 v83, v83, v80, v81
	v_max3_f32 v82, v82, v79, v62
	v_max3_f32 v83, v83, v64, v65
	v_max3_f32 v82, v82, v63, v83
	v_add_f32_e32 v183, v198, v84
	s_add_u32 s54, s52, 0x2000
	s_addc_u32 s55, s53, 0
	s_add_i32 s26, s43, s35
	s_mov_b32 m0, s26
	s_nop 0
	global_load_lds_dwordx4 v222, s[54:55]
	v_cmp_lt_f32_e32 vcc, s41, v82
	s_cmp_lg_u64 vcc, 0
	s_cselect_b64 s[26:27], -1, 0
	s_cbranch_vccnz .Lu2_12

	.amdhsa_kernel _ZN4attn8attn_fwdEPKDF16_PDF16_
		.amdhsa_group_segment_fixed_size 83968
		.amdhsa_private_segment_fixed_size 0
		.amdhsa_kernarg_size 16
		.amdhsa_user_sgpr_count 2
		.amdhsa_user_sgpr_dispatch_ptr 0
		.amdhsa_user_sgpr_queue_ptr 0
		.amdhsa_user_sgpr_kernarg_segment_ptr 1
		.amdhsa_user_sgpr_dispatch_id 0
		.amdhsa_user_sgpr_kernarg_preload_length 0
		.amdhsa_user_sgpr_kernarg_preload_offset 0
		.amdhsa_user_sgpr_private_segment_size 0
		.amdhsa_uses_dynamic_stack 0
		.amdhsa_enable_private_segment 0
		.amdhsa_system_sgpr_workgroup_id_x 1
		.amdhsa_system_sgpr_workgroup_id_y 0
		.amdhsa_system_sgpr_workgroup_id_z 0
		.amdhsa_system_sgpr_workgroup_info 0
		.amdhsa_system_vgpr_workitem_id 0
		.amdhsa_next_free_vgpr 232
		.amdhsa_next_free_sgpr 96
		.amdhsa_accum_offset 232
		.amdhsa_reserve_vcc 1
		.amdhsa_float_round_mode_32 0
		.amdhsa_float_round_mode_16_64 0
		.amdhsa_float_denorm_mode_32 3
		.amdhsa_float_denorm_mode_16_64 3
		.amdhsa_dx10_clamp 1
		.amdhsa_ieee_mode 1
		.amdhsa_fp16_overflow 0
		.amdhsa_tg_split 0
		.amdhsa_exception_fp_ieee_invalid_op 0
		.amdhsa_exception_fp_denorm_src 0
		.amdhsa_exception_fp_ieee_div_zero 0
		.amdhsa_exception_fp_ieee_overflow 0
		.amdhsa_exception_fp_ieee_underflow 0
		.amdhsa_exception_fp_ieee_inexact 0
		.amdhsa_exception_int_div_zero 0
	.end_amdhsa_kernel
